# k_finalize: five predicated head loads issued back to back with pre-zeroed destinations, one wait, branch-free conversions (on top of hoisted upsample stores)
# speedup vs baseline: 1.0100x; 1.0026x over previous
_Z10k_finalizePKfiS0_iPf:
	s_load_dword s12, s[0:1], 0x8
	s_load_dwordx2 s[2:3], s[0:1], 0x0
	s_load_dword s14, s[0:1], 0x18
	s_load_dwordx2 s[4:5], s[0:1], 0x10
	v_lshlrev_b32_e32 v6, 4, v0
	v_or_b32_e32 v1, 0x400, v0
	v_or_b32_e32 v24, 0x800, v0
	v_or_b32_e32 v25, 0xc00, v0
	v_lshlrev_b32_e32 v8, 2, v0
	v_mov_b32_e32 v14, 0
	v_mov_b32_e32 v15, 0
	v_mov_b32_e32 v16, 0
	v_mov_b32_e32 v17, 0
	v_mov_b32_e32 v20, 0
	v_mov_b32_e32 v21, 0
	v_mov_b32_e32 v22, 0
	v_mov_b32_e32 v23, 0
	v_mov_b32_e32 v34, 0
	v_mov_b32_e32 v35, 0
	v_mov_b32_e32 v36, 0
	v_mov_b32_e32 v37, 0
	v_mov_b32_e32 v40, 0
	v_mov_b32_e32 v41, 0
	v_mov_b32_e32 v42, 0
	v_mov_b32_e32 v43, 0
	v_mov_b32_e32 v2, 0
	v_lshlrev_b32_e32 v28, 4, v1
	v_lshlrev_b32_e32 v26, 4, v24
	v_lshlrev_b32_e32 v27, 4, v25
	s_waitcnt lgkmcnt(0)
	s_ashr_i32 s13, s12, 2
	v_cmp_gt_i32_e32 vcc, s13, v0
	s_and_saveexec_b64 s[6:7], vcc
	global_load_dwordx4 v[14:17], v6, s[2:3]
	s_mov_b64 exec, s[6:7]
	v_cmp_gt_i32_e32 vcc, s13, v1
	s_and_saveexec_b64 s[6:7], vcc
	global_load_dwordx4 v[20:23], v28, s[2:3]
	s_mov_b64 exec, s[6:7]
	v_cmp_gt_i32_e32 vcc, s13, v24
	s_and_saveexec_b64 s[6:7], vcc
	global_load_dwordx4 v[34:37], v26, s[2:3]
	s_mov_b64 exec, s[6:7]
	v_cmp_gt_i32_e32 vcc, s13, v25
	s_and_saveexec_b64 s[6:7], vcc
	global_load_dwordx4 v[40:43], v27, s[2:3]
	s_mov_b64 exec, s[6:7]
	v_cmp_gt_i32_e32 vcc, s14, v0
	s_and_saveexec_b64 s[6:7], vcc
	global_load_dword v2, v8, s[4:5]
	s_mov_b64 exec, s[6:7]
	s_waitcnt vmcnt(0)
	v_cvt_f64_f32_e32 v[10:11], v14
	v_cvt_f64_f32_e32 v[12:13], v15
	v_cvt_f64_f32_e32 v[14:15], v16
	v_cvt_f64_f32_e32 v[16:17], v17
	v_cvt_f64_f32_e32 v[18:19], v20
	v_cvt_f64_f32_e32 v[4:5], v21
	v_cvt_f64_f32_e32 v[20:21], v22
	v_cvt_f64_f32_e32 v[22:23], v23
	v_cvt_f64_f32_e32 v[32:33], v34
	v_cvt_f64_f32_e32 v[30:31], v35
	v_cvt_f64_f32_e32 v[28:29], v36
	v_cvt_f64_f32_e32 v[26:27], v37
	v_cvt_f64_f32_e32 v[34:35], v42
	v_cvt_f64_f32_e32 v[38:39], v40
	v_cvt_f64_f32_e32 v[24:25], v43
	v_cvt_f64_f32_e32 v[36:37], v41
	v_cvt_f64_f32_e32 v[2:3], v2
	v_add_f64 v[10:11], v[10:11], v[12:13]
	v_add_f64 v[12:13], v[14:15], v[16:17]
	v_add_f64 v[10:11], v[10:11], v[12:13]
	v_add_f64 v[4:5], v[4:5], v[18:19]
	v_add_f64 v[4:5], v[10:11], v[4:5]
	v_add_f64 v[10:11], v[20:21], v[22:23]
	s_load_dwordx2 s[0:1], s[0:1], 0x20
	v_add_f64 v[4:5], v[4:5], v[10:11]
	v_add_f64 v[10:11], v[30:31], v[32:33]
	v_add_f64 v[4:5], v[4:5], v[10:11]
	v_add_f64 v[10:11], v[26:27], v[28:29]
	v_add_f64 v[4:5], v[10:11], v[4:5]
	v_add_f64 v[12:13], v[36:37], v[38:39]
	v_add_f64 v[10:11], v[24:25], v[34:35]
	v_add_f64 v[4:5], v[4:5], v[12:13]
	v_or_b32_e32 v9, 0x1000, v0
	v_add_f64 v[4:5], v[10:11], v[4:5]
	v_cmp_gt_i32_e32 vcc, s13, v9
	s_and_saveexec_b64 s[6:7], vcc
	s_cbranch_execz .LBB3_14
	v_mov_b32_e32 v7, 0
	v_lshl_add_u64 v[6:7], s[2:3], 0, v[6:7]
	s_mov_b64 s[8:9], 0x10000
	v_lshl_add_u64 v[6:7], v[6:7], 0, s[8:9]
	s_mov_b64 s[8:9], 0
	s_mov_b64 s[10:11], 0x4000
